# select phase: rsC gathered with two dwordx4 loads at item start instead of 8 serialized load-wait-store steps
# baseline (speedup 1.0000x reference)
; #define BID() lnd_s((int)blockIdx.x)
; #define NBLK() lnd_s((int)gridDim.x)
; __device__ __forceinline__ void phase_select(const int wv_, KP p, unsigned char* lds) {
;     ...
;     for (int item = BID(); item < NB * NE; item += NBLK()) {
;         const int par = 0; const int b = item >> 4, e = item & 15;
;         const float* a = aff + (size_t)item * SEQ + tid * 8;
;         const f32x4 v0 = *(const f32x4*)a, v1 = *(const f32x4*)(a + 4);
;         float v[8] = {v0[0], v0[1], v0[2], v0[3], v1[0], v1[1], v1[2], v1[3]}; unsigned bits[8];
;     ...
;             if (pos >= 0) { tok[(size_t)item * CAP + pos] = s; gate[(size_t)item * CAP + pos] = v[i]; rsrow[(size_t)item * CAP + pos] = rsC[b * SEQ + s]; } }
.LBB0_1396:
	s_ashr_i32 s21, s20, 31
	s_lshl_b64 s[0:1], s[20:21], 14
	v_lshl_add_u64 v[4:5], v[18:19], 0, s[0:1]
	global_load_dwordx4 v[0:3], v[4:5], off offset:16
	s_nop 0
	global_load_dwordx4 v[4:7], v[4:5], off
	s_ashr_i32 s98, s20, 4
	s_lshl_b32 s98, s98, 14
	s_add_u32 s98, s2, s98
	s_addc_u32 s99, s3, 0
	v_lshl_add_u64 v[64:65], v[16:17], 2, s[98:99]
	global_load_dwordx4 v[68:71], v[64:65], off
	global_load_dwordx4 v[72:75], v[64:65], off offset:16
	s_mov_b32 s0, 30
	s_movk_i32 s1, 0xf0
	v_mov_b32_e32 v35, 0
	s_branch .LBB0_1398

; __device__ __forceinline__ void phase_select(const int wv_, KP p, unsigned char* lds) {
;     ...
;         unsigned cg = 0, ce = 0;
; #pragma unroll
;         for (int i = 0; i < 8; ++i) { cg += bits[i] > thr ? 1u : 0u; ce += bits[i] == thr ? 1u : 0u; }
;         unsigned pk = cg | (ce << 16), incl = pk;
; #pragma unroll
;         for (int o = 1; o < 64; o <<= 1) { const unsigned y = (unsigned)__builtin_amdgcn_ds_bpermute((lane - o) << 2, (int)incl); if (lane >= o) incl += y; }
;         __syncthreads();
;         if (lane == 63) wtot[wid] = incl;
;         __syncthreads();
;         unsigned base = 0;
; #pragma unroll
;         for (int w = 0; w < 8; ++w) base += (w < wid) ? wtot[w] : 0u;
;         const unsigned ex = base + incl - pk; unsigned gb = ex & 0xffffu, eb = ex >> 16;
; #pragma unroll
;         for (int i = 0; i < 8; ++i) { const int s = tid * 8 + i; int pos = -1;
;             if (bits[i] > thr) { pos = (int)(gb + (eb < need ? eb : need)); ++gb; }
;             else if (bits[i] == thr) { if (eb < need) pos = (int)(gb + eb); ++eb; }
;             if (par == 0) slot[((size_t)b * SEQ + s) * NE + e] = pos;
;             if (pos >= 0) { tok[(size_t)item * CAP + pos] = s; gate[(size_t)item * CAP + pos] = v[i]; rsrow[(size_t)item * CAP + pos] = rsC[b * SEQ + s]; } }
.LBB0_1402:
	s_or_b64 exec, exec, s[0:1]
	v_cndmask_b32_e64 v17, 0, 1, s[94:95]
	v_cndmask_b32_e64 v23, 0, 1, s[90:91]
	v_cmp_eq_u32_e64 s[90:91], v5, v35
	v_cmp_eq_u32_e64 s[94:95], v4, v35
	v_add_u32_e32 v17, v17, v23
	v_cndmask_b32_e64 v31, 0, 1, s[90:91]
	v_cndmask_b32_e64 v39, 0, 1, s[88:89]
	v_cmp_eq_u32_e64 s[88:89], v6, v35
	v_cndmask_b32_e64 v43, 0, 1, s[84:85]
	v_addc_co_u32_e64 v23, vcc, 0, v31, s[94:95]
	v_cndmask_b32_e64 v27, 0, 1, s[88:89]
	v_add3_u32 v17, v17, v39, v43
	v_cmp_eq_u32_e64 s[84:85], v7, v35
	v_cndmask_b32_e64 v43, 0, 1, s[80:81]
	v_cmp_eq_u32_e64 s[80:81], v0, v35
	v_cndmask_b32_e64 v47, 0, 1, s[76:77]
	v_addc_co_u32_e64 v39, vcc, v23, v27, s[84:85]
	v_cndmask_b32_e64 v23, 0, 1, s[80:81]
	v_add3_u32 v43, v17, v43, v47
	v_cmp_eq_u32_e64 s[76:77], v1, v35
	v_cndmask_b32_e64 v47, 0, 1, s[72:73]
	v_cmp_eq_u32_e64 s[72:73], v2, v35
	v_addc_co_u32_e64 v39, vcc, v39, v23, s[76:77]
	s_nop 0
	v_cndmask_b32_e64 v17, 0, 1, s[72:73]
	v_cndmask_b32_e64 v58, 0, 1, s[68:69]
	v_cmp_eq_u32_e64 s[68:69], v3, v35
	v_add3_u32 v43, v43, v47, v58
	s_waitcnt lgkmcnt(0)
	v_addc_co_u32_e64 v35, vcc, v39, v17, s[68:69]
	v_lshl_or_b32 v35, v35, 16, v43
	ds_bpermute_b32 v39, v52, v35
	s_barrier
	s_waitcnt lgkmcnt(0)
	ds_read_b128 v[12:15], v97 offset:1088
	ds_read_b128 v[8:11], v97 offset:1104
	s_waitcnt lgkmcnt(0)
	v_cndmask_b32_e64 v39, v39, 0, s[96:97]
	v_add_u32_e32 v39, v39, v35
	ds_bpermute_b32 v43, v53, v39
	s_barrier
	s_waitcnt lgkmcnt(0)
	v_cndmask_b32_e64 v43, v43, 0, s[38:39]
	v_add_u32_e32 v39, v43, v39
	ds_bpermute_b32 v43, v54, v39
	s_waitcnt lgkmcnt(0)
	v_cndmask_b32_e64 v43, v43, 0, s[40:41]
	v_add_u32_e32 v39, v43, v39
	ds_bpermute_b32 v43, v55, v39
	s_waitcnt lgkmcnt(0)
	v_cndmask_b32_e64 v43, v43, 0, s[42:43]
	v_add_u32_e32 v39, v43, v39
	ds_bpermute_b32 v43, v56, v39
	s_waitcnt lgkmcnt(0)
	v_cndmask_b32_e64 v43, v43, 0, s[44:45]
	v_add_u32_e32 v39, v43, v39
	ds_bpermute_b32 v43, v57, v39
	s_waitcnt lgkmcnt(0)
	v_cndmask_b32_e64 v43, v43, 0, s[46:47]
	v_add_u32_e32 v39, v43, v39
	s_and_saveexec_b64 s[0:1], s[36:37]
	ds_write_b32 v51, v39 offset:1024
	s_or_b64 exec, exec, s[0:1]
	v_mov_b32_e32 v43, 0
	v_mov_b32_e32 v47, 0
	s_waitcnt lgkmcnt(0)
	s_barrier
	s_and_saveexec_b64 s[0:1], s[48:49]
	ds_read_b32 v47, v97 offset:1024
	s_or_b64 exec, exec, s[0:1]
	s_and_saveexec_b64 s[0:1], s[50:51]
	ds_read_b32 v43, v97 offset:1028
	s_or_b64 exec, exec, s[0:1]
	v_mov_b32_e32 v58, 0
	v_mov_b32_e32 v59, 0
	s_and_saveexec_b64 s[0:1], s[52:53]
	ds_read_b32 v59, v97 offset:1032
	s_or_b64 exec, exec, s[0:1]
	s_and_saveexec_b64 s[0:1], s[54:55]
	ds_read_b32 v58, v97 offset:1036
	s_or_b64 exec, exec, s[0:1]
	v_mov_b32_e32 v60, 0
	v_mov_b32_e32 v61, 0
	s_and_saveexec_b64 s[0:1], s[56:57]
	ds_read_b32 v61, v97 offset:1040
	s_or_b64 exec, exec, s[0:1]
	s_and_saveexec_b64 s[0:1], s[58:59]
	ds_read_b32 v60, v97 offset:1044
	s_or_b64 exec, exec, s[0:1]
	v_mov_b32_e32 v62, 0
	v_mov_b32_e32 v63, 0
	s_and_saveexec_b64 s[0:1], s[60:61]
	ds_read_b32 v63, v97 offset:1048
	s_or_b64 exec, exec, s[0:1]
	s_and_saveexec_b64 s[0:1], s[62:63]
	ds_read_b32 v62, v97 offset:1052
	s_or_b64 exec, exec, s[0:1]
	v_add_u32_e32 v12, v12, v13
	v_add_u32_e32 v12, v12, v14
	v_add_u32_e32 v12, v12, v15
	v_add_u32_e32 v8, v12, v8
	v_add_u32_e32 v8, v8, v9
	v_sub_u32_e32 v9, v39, v35
	s_waitcnt lgkmcnt(0)
	v_add3_u32 v9, v47, v9, v43
	v_add3_u32 v9, v9, v59, v58
	v_add_u32_e32 v8, v8, v10
	v_add3_u32 v9, v9, v61, v60
	v_add_u32_e32 v8, v8, v11
	v_add3_u32 v10, v9, v63, v62
	v_sub_u32_e32 v8, 0x200, v8
	v_and_b32_e32 v9, 0xffff, v10
	v_lshrrev_b32_e32 v10, 16, v10
	s_and_saveexec_b64 s[0:1], s[92:93]
	s_xor_b64 s[0:1], exec, s[0:1]
	v_cmp_lt_u32_e32 vcc, v10, v8
	v_cndmask_b32_e64 v11, 0, 1, s[94:95]
	v_add_u32_e32 v12, v10, v9
	s_and_b64 vcc, s[94:95], vcc
	v_add_u32_e32 v10, v10, v11
	v_cndmask_b32_e32 v96, -1, v12, vcc
	s_andn2_saveexec_b64 s[0:1], s[0:1]
	v_min_u32_e32 v11, v10, v8
	v_add_u32_e32 v96, v11, v9
	v_add_u32_e32 v9, 1, v9
	s_or_b64 exec, exec, s[0:1]
	s_waitcnt vmcnt(0)
	s_ashr_i32 s0, s20, 4
	s_ashr_i32 s1, s0, 31
	s_and_b32 s94, s20, 15
	s_lshl_b64 s[92:93], s[0:1], 18
	s_add_u32 s1, s26, s92
	s_addc_u32 s92, s29, s93
	s_lshl_b32 s93, s94, 2
	s_add_u32 s94, s1, s93
	s_addc_u32 s95, s92, 0
	s_lshl_b64 s[92:93], s[20:21], 9
	s_lshl_b32 s21, s0, 12
	v_lshl_add_u64 v[12:13], s[94:95], 0, v[20:21]
	v_cmp_lt_i32_e32 vcc, -1, v96
	global_store_dword v[12:13], v96, off
	s_and_saveexec_b64 s[0:1], vcc
	s_cbranch_execz .LBB0_1454
	v_lshl_add_u64 v[12:13], s[92:93], 0, v[96:97]
	v_lshlrev_b64 v[12:13], 2, v[12:13]
	v_lshl_add_u64 v[14:15], s[24:25], 0, v[12:13]
	global_store_dword v[14:15], v4, off
	v_add_u32_e32 v14, s21, v16
	v_ashrrev_i32_e32 v15, 31, v14
	v_lshl_add_u64 v[14:15], v[14:15], 2, s[2:3]
	v_mov_b32_e32 v4, v68
	v_lshl_add_u64 v[14:15], s[4:5], 0, v[12:13]
	v_lshl_add_u64 v[12:13], s[22:23], 0, v[12:13]
	global_store_dword v[14:15], v16, off
	global_store_dword v[12:13], v4, off
	s_or_b64 exec, exec, s[0:1]
	s_and_saveexec_b64 s[0:1], s[86:87]
	s_xor_b64 s[0:1], exec, s[0:1]
	s_cbranch_execnz .LBB0_1455

; __device__ __forceinline__ void phase_select(const int wv_, KP p, unsigned char* lds) {
;     ...
;         for (int i = 0; i < 8; ++i) { const int s = tid * 8 + i; int pos = -1;
;             if (bits[i] > thr) { pos = (int)(gb + (eb < need ? eb : need)); ++gb; }
;             else if (bits[i] == thr) { if (eb < need) pos = (int)(gb + eb); ++eb; }
;             if (par == 0) slot[((size_t)b * SEQ + s) * NE + e] = pos;
;             if (pos >= 0) { tok[(size_t)item * CAP + pos] = s; gate[(size_t)item * CAP + pos] = v[i]; rsrow[(size_t)item * CAP + pos] = rsC[b * SEQ + s]; } }
.LBB0_1428:
	s_or_b64 exec, exec, s[0:1]
	v_lshl_add_u64 v[12:13], s[94:95], 0, v[24:25]
	v_cmp_lt_i32_e32 vcc, -1, v96
	global_store_dword v[12:13], v96, off
	s_and_saveexec_b64 s[0:1], vcc
	s_cbranch_execz .LBB0_1456
	v_lshl_add_u64 v[12:13], s[92:93], 0, v[96:97]
	v_lshlrev_b64 v[12:13], 2, v[12:13]
	v_lshl_add_u64 v[14:15], s[24:25], 0, v[12:13]
	v_add_u32_e32 v4, s21, v22
	global_store_dword v[14:15], v5, off
	v_ashrrev_i32_e32 v5, 31, v4
	v_lshl_add_u64 v[4:5], v[4:5], 2, s[2:3]
	v_mov_b32_e32 v11, v69
	v_lshl_add_u64 v[4:5], s[4:5], 0, v[12:13]
	global_store_dword v[4:5], v22, off
	v_lshl_add_u64 v[4:5], s[22:23], 0, v[12:13]
	global_store_dword v[4:5], v11, off
	s_or_b64 exec, exec, s[0:1]
	s_and_saveexec_b64 s[0:1], s[82:83]
	s_xor_b64 s[0:1], exec, s[0:1]
	s_cbranch_execnz .LBB0_1457

; __device__ __forceinline__ void phase_select(const int wv_, KP p, unsigned char* lds) {
;     ...
;         for (int i = 0; i < 8; ++i) { const int s = tid * 8 + i; int pos = -1;
;             if (bits[i] > thr) { pos = (int)(gb + (eb < need ? eb : need)); ++gb; }
;             else if (bits[i] == thr) { if (eb < need) pos = (int)(gb + eb); ++eb; }
;             if (par == 0) slot[((size_t)b * SEQ + s) * NE + e] = pos;
;             if (pos >= 0) { tok[(size_t)item * CAP + pos] = s; gate[(size_t)item * CAP + pos] = v[i]; rsrow[(size_t)item * CAP + pos] = rsC[b * SEQ + s]; } }
.LBB0_1432:
	s_or_b64 exec, exec, s[0:1]
	v_lshl_add_u64 v[4:5], s[94:95], 0, v[28:29]
	v_cmp_lt_i32_e32 vcc, -1, v96
	global_store_dword v[4:5], v96, off
	s_and_saveexec_b64 s[0:1], vcc
	s_cbranch_execz .LBB0_1458
	v_lshl_add_u64 v[4:5], s[92:93], 0, v[96:97]
	v_lshlrev_b64 v[4:5], 2, v[4:5]
	v_lshl_add_u64 v[12:13], s[24:25], 0, v[4:5]
	global_store_dword v[12:13], v6, off
	v_add_u32_e32 v12, s21, v26
	v_ashrrev_i32_e32 v13, 31, v12
	v_lshl_add_u64 v[12:13], v[12:13], 2, s[2:3]
	v_mov_b32_e32 v6, v70
	v_lshl_add_u64 v[12:13], s[4:5], 0, v[4:5]
	v_lshl_add_u64 v[4:5], s[22:23], 0, v[4:5]
	global_store_dword v[12:13], v26, off
	global_store_dword v[4:5], v6, off
	s_or_b64 exec, exec, s[0:1]
	s_and_saveexec_b64 s[0:1], s[78:79]
	s_xor_b64 s[0:1], exec, s[0:1]
	s_cbranch_execnz .LBB0_1459

; __device__ __forceinline__ void phase_select(const int wv_, KP p, unsigned char* lds) {
;     ...
;         for (int i = 0; i < 8; ++i) { const int s = tid * 8 + i; int pos = -1;
;             if (bits[i] > thr) { pos = (int)(gb + (eb < need ? eb : need)); ++gb; }
;             else if (bits[i] == thr) { if (eb < need) pos = (int)(gb + eb); ++eb; }
;             if (par == 0) slot[((size_t)b * SEQ + s) * NE + e] = pos;
;             if (pos >= 0) { tok[(size_t)item * CAP + pos] = s; gate[(size_t)item * CAP + pos] = v[i]; rsrow[(size_t)item * CAP + pos] = rsC[b * SEQ + s]; } }
.LBB0_1436:
	s_or_b64 exec, exec, s[0:1]
	v_lshl_add_u64 v[4:5], s[94:95], 0, v[32:33]
	v_cmp_lt_i32_e32 vcc, -1, v96
	global_store_dword v[4:5], v96, off
	s_and_saveexec_b64 s[0:1], vcc
	s_cbranch_execz .LBB0_1460
	v_lshl_add_u64 v[4:5], s[92:93], 0, v[96:97]
	v_lshlrev_b64 v[4:5], 2, v[4:5]
	v_lshl_add_u64 v[12:13], s[24:25], 0, v[4:5]
	v_add_u32_e32 v6, s21, v30
	global_store_dword v[12:13], v7, off
	v_ashrrev_i32_e32 v7, 31, v6
	v_lshl_add_u64 v[6:7], v[6:7], 2, s[2:3]
	v_mov_b32_e32 v11, v71
	v_lshl_add_u64 v[6:7], s[4:5], 0, v[4:5]
	v_lshl_add_u64 v[4:5], s[22:23], 0, v[4:5]
	global_store_dword v[6:7], v30, off
	global_store_dword v[4:5], v11, off
	s_or_b64 exec, exec, s[0:1]
	s_and_saveexec_b64 s[0:1], s[74:75]
	s_xor_b64 s[0:1], exec, s[0:1]
	s_cbranch_execnz .LBB0_1461

; __device__ __forceinline__ void phase_select(const int wv_, KP p, unsigned char* lds) {
;     ...
;         for (int i = 0; i < 8; ++i) { const int s = tid * 8 + i; int pos = -1;
;             if (bits[i] > thr) { pos = (int)(gb + (eb < need ? eb : need)); ++gb; }
;             else if (bits[i] == thr) { if (eb < need) pos = (int)(gb + eb); ++eb; }
;             if (par == 0) slot[((size_t)b * SEQ + s) * NE + e] = pos;
;             if (pos >= 0) { tok[(size_t)item * CAP + pos] = s; gate[(size_t)item * CAP + pos] = v[i]; rsrow[(size_t)item * CAP + pos] = rsC[b * SEQ + s]; } }
.LBB0_1440:
	s_or_b64 exec, exec, s[0:1]
	v_lshl_add_u64 v[4:5], s[94:95], 0, v[36:37]
	v_cmp_lt_i32_e32 vcc, -1, v96
	global_store_dword v[4:5], v96, off
	s_and_saveexec_b64 s[0:1], vcc
	s_cbranch_execz .LBB0_1462
	v_lshl_add_u64 v[4:5], s[92:93], 0, v[96:97]
	v_lshlrev_b64 v[4:5], 2, v[4:5]
	v_lshl_add_u64 v[6:7], s[24:25], 0, v[4:5]
	global_store_dword v[6:7], v0, off
	v_add_u32_e32 v6, s21, v34
	v_ashrrev_i32_e32 v7, 31, v6
	v_lshl_add_u64 v[6:7], v[6:7], 2, s[2:3]
	v_mov_b32_e32 v0, v72
	v_lshl_add_u64 v[6:7], s[4:5], 0, v[4:5]
	v_lshl_add_u64 v[4:5], s[22:23], 0, v[4:5]
	global_store_dword v[6:7], v34, off
	global_store_dword v[4:5], v0, off
	s_or_b64 exec, exec, s[0:1]
	s_and_saveexec_b64 s[0:1], s[70:71]
	s_xor_b64 s[0:1], exec, s[0:1]
	s_cbranch_execnz .LBB0_1463

; __device__ __forceinline__ void phase_select(const int wv_, KP p, unsigned char* lds) {
;     ...
;         for (int i = 0; i < 8; ++i) { const int s = tid * 8 + i; int pos = -1;
;             if (bits[i] > thr) { pos = (int)(gb + (eb < need ? eb : need)); ++gb; }
;             else if (bits[i] == thr) { if (eb < need) pos = (int)(gb + eb); ++eb; }
;             if (par == 0) slot[((size_t)b * SEQ + s) * NE + e] = pos;
;             if (pos >= 0) { tok[(size_t)item * CAP + pos] = s; gate[(size_t)item * CAP + pos] = v[i]; rsrow[(size_t)item * CAP + pos] = rsC[b * SEQ + s]; } }
.LBB0_1444:
	s_or_b64 exec, exec, s[0:1]
	v_lshl_add_u64 v[4:5], s[94:95], 0, v[40:41]
	v_cmp_lt_i32_e32 vcc, -1, v96
	global_store_dword v[4:5], v96, off
	s_and_saveexec_b64 s[0:1], vcc
	s_cbranch_execz .LBB0_1464
	v_lshl_add_u64 v[4:5], s[92:93], 0, v[96:97]
	v_lshlrev_b64 v[4:5], 2, v[4:5]
	v_lshl_add_u64 v[6:7], s[24:25], 0, v[4:5]
	v_add_u32_e32 v0, s21, v38
	global_store_dword v[6:7], v1, off
	v_ashrrev_i32_e32 v1, 31, v0
	v_lshl_add_u64 v[0:1], v[0:1], 2, s[2:3]
	v_mov_b32_e32 v6, v73
	v_lshl_add_u64 v[0:1], s[4:5], 0, v[4:5]
	global_store_dword v[0:1], v38, off
	v_lshl_add_u64 v[0:1], s[22:23], 0, v[4:5]
	global_store_dword v[0:1], v6, off
	s_or_b64 exec, exec, s[0:1]
	s_and_saveexec_b64 s[0:1], s[66:67]
	s_xor_b64 s[0:1], exec, s[0:1]
	s_cbranch_execnz .LBB0_1465

; __device__ __forceinline__ void phase_select(const int wv_, KP p, unsigned char* lds) {
;     ...
;         for (int i = 0; i < 8; ++i) { const int s = tid * 8 + i; int pos = -1;
;             if (bits[i] > thr) { pos = (int)(gb + (eb < need ? eb : need)); ++gb; }
;             else if (bits[i] == thr) { if (eb < need) pos = (int)(gb + eb); ++eb; }
;             if (par == 0) slot[((size_t)b * SEQ + s) * NE + e] = pos;
;             if (pos >= 0) { tok[(size_t)item * CAP + pos] = s; gate[(size_t)item * CAP + pos] = v[i]; rsrow[(size_t)item * CAP + pos] = rsC[b * SEQ + s]; } }
.LBB0_1448:
	s_or_b64 exec, exec, s[0:1]
	v_lshl_add_u64 v[0:1], s[94:95], 0, v[44:45]
	v_cmp_lt_i32_e32 vcc, -1, v96
	global_store_dword v[0:1], v96, off
	s_and_saveexec_b64 s[0:1], vcc
	s_cbranch_execz .LBB0_1466
	v_lshl_add_u64 v[0:1], s[92:93], 0, v[96:97]
	v_lshlrev_b64 v[0:1], 2, v[0:1]
	v_lshl_add_u64 v[4:5], s[24:25], 0, v[0:1]
	global_store_dword v[4:5], v2, off
	v_add_u32_e32 v4, s21, v42
	v_ashrrev_i32_e32 v5, 31, v4
	v_lshl_add_u64 v[4:5], v[4:5], 2, s[2:3]
	v_mov_b32_e32 v2, v74
	v_lshl_add_u64 v[4:5], s[4:5], 0, v[0:1]
	v_lshl_add_u64 v[0:1], s[22:23], 0, v[0:1]
	global_store_dword v[4:5], v42, off
	global_store_dword v[0:1], v2, off
	s_or_b64 exec, exec, s[0:1]
	s_and_saveexec_b64 s[0:1], s[64:65]
	s_xor_b64 s[0:1], exec, s[0:1]
	s_cbranch_execnz .LBB0_1467

; __device__ __forceinline__ void phase_select(const int wv_, KP p, unsigned char* lds) {
;     ...
;         for (int i = 0; i < 8; ++i) { const int s = tid * 8 + i; int pos = -1;
;             if (bits[i] > thr) { pos = (int)(gb + (eb < need ? eb : need)); ++gb; }
;             else if (bits[i] == thr) { if (eb < need) pos = (int)(gb + eb); ++eb; }
;             if (par == 0) slot[((size_t)b * SEQ + s) * NE + e] = pos;
;             if (pos >= 0) { tok[(size_t)item * CAP + pos] = s; gate[(size_t)item * CAP + pos] = v[i]; rsrow[(size_t)item * CAP + pos] = rsC[b * SEQ + s]; } }
.LBB0_1452:
	s_or_b64 exec, exec, s[0:1]
	v_lshl_add_u64 v[0:1], s[94:95], 0, v[48:49]
	v_cmp_lt_i32_e32 vcc, -1, v96
	global_store_dword v[0:1], v96, off
	s_and_saveexec_b64 s[0:1], vcc
	s_cbranch_execz .LBB0_1395
	v_lshl_add_u64 v[0:1], s[92:93], 0, v[96:97]
	v_lshlrev_b64 v[0:1], 2, v[0:1]
	v_lshl_add_u64 v[4:5], s[24:25], 0, v[0:1]
	v_add_u32_e32 v2, s21, v46
	global_store_dword v[4:5], v3, off
	v_ashrrev_i32_e32 v3, 31, v2
	v_lshl_add_u64 v[2:3], v[2:3], 2, s[2:3]
	v_mov_b32_e32 v4, v75
	v_lshl_add_u64 v[2:3], s[4:5], 0, v[0:1]
	v_lshl_add_u64 v[0:1], s[22:23], 0, v[0:1]
	global_store_dword v[2:3], v46, off
	global_store_dword v[0:1], v4, off
	s_branch .LBB0_1395
